# speedup vs baseline: 1.0018x; 1.0018x over previous
.Llight_path:
	s_waitcnt vmcnt(16)
	v_mul_u32_u24_e32 v236, 36, v228
	v_add_u32_e32 v236, v236, v230
	v_add_u32_e32 v237, s7, v229
	v_mul_u32_u24_e32 v238, 0x104, v228
	v_add_u32_e32 v238, v238, v237
	v_add_u32_e32 v238, 0xb840, v238
	v_add_u32_e32 v231, s7, v229
	v_add_u32_e32 v231, 0xb840, v231
	v_add_u32_e32 v211, s6, v210
	s_nop 0
	s_load_dwordx8 s[4:11], s[0:1], 0x10
	v_add_u32_e32 v232, 0x24e80, v228
	ds_read_b32 v244, v232
	ds_read_b32 v245, v232 offset:128
	ds_read_b128 v[194:197], v237 offset:36928
	ds_read_b128 v[198:201], v237 offset:36944
	ds_read_b128 v[202:205], v237 offset:36960
	ds_read_b128 v[206:209], v237 offset:36976
	ds_read_b128 v[212:215], v237 offset:37056
	ds_read_b128 v[216:219], v237 offset:37072
	ds_read_b128 v[220:223], v237 offset:37088
	ds_read_b128 v[224:227], v237 offset:37104
	ds_read_b128 v[162:165], v236 offset:16384
	ds_read_b128 v[166:169], v236 offset:16416
	ds_read_b128 v[170:173], v236 offset:16448
	ds_read_b128 v[174:177], v236 offset:16480
	s_waitcnt lgkmcnt(0)
	v_mfma_f32_32x32x16_bf16 v[2:17], v[94:97], v[162:165], v[194:209]
	v_mfma_f32_32x32x16_bf16 v[18:33], v[46:49], v[162:165], v[212:227]
	v_mfma_f32_32x32x16_bf16 v[2:17], v[90:93], v[166:169], v[2:17]
	v_mfma_f32_32x32x16_bf16 v[18:33], v[42:45], v[166:169], v[18:33]
	v_mfma_f32_32x32x16_bf16 v[2:17], v[86:89], v[170:173], v[2:17]
	ds_read_b128 v[178:181], v236 offset:20992
	v_mfma_f32_32x32x16_bf16 v[18:33], v[38:41], v[170:173], v[18:33]
	ds_read_b128 v[182:185], v236 offset:21024
	v_mfma_f32_32x32x16_bf16 v[2:17], v[82:85], v[174:177], v[2:17]
	ds_read_b128 v[186:189], v236 offset:21056
	v_mfma_f32_32x32x16_bf16 v[18:33], v[34:37], v[174:177], v[18:33]
	ds_read_b128 v[190:193], v236 offset:21088
	s_waitcnt lgkmcnt(0)
	v_mfma_f32_32x32x16_bf16 v[130:145], v[94:97], v[178:181], v[194:209]
	v_mfma_f32_32x32x16_bf16 v[146:161], v[46:49], v[178:181], v[212:227]
	v_mfma_f32_32x32x16_bf16 v[130:145], v[90:93], v[182:185], v[130:145]
	v_mfma_f32_32x32x16_bf16 v[146:161], v[42:45], v[182:185], v[146:161]
	s_nop 7
	ds_write_b128 v238, v[2:5] offset:0
	ds_write_b128 v238, v[6:9] offset:16
	ds_write_b128 v238, v[10:13] offset:32
	ds_write_b128 v238, v[14:17] offset:48
	ds_write_b128 v238, v[18:21] offset:128
	ds_write_b128 v238, v[22:25] offset:144
	ds_write_b128 v238, v[26:29] offset:160
	ds_write_b128 v238, v[30:33] offset:176
	v_mfma_f32_32x32x16_bf16 v[130:145], v[86:89], v[186:189], v[130:145]
	ds_read_b128 v[162:165], v236 offset:25600
	v_mfma_f32_32x32x16_bf16 v[146:161], v[38:41], v[186:189], v[146:161]
	ds_read_b128 v[166:169], v236 offset:25632
	v_mfma_f32_32x32x16_bf16 v[130:145], v[82:85], v[190:193], v[130:145]
	ds_read_b128 v[170:173], v236 offset:25664
	v_mfma_f32_32x32x16_bf16 v[146:161], v[34:37], v[190:193], v[146:161]
	ds_read_b128 v[174:177], v236 offset:25696
	s_waitcnt lgkmcnt(0)
	v_mfma_f32_32x32x16_bf16 v[2:17], v[94:97], v[162:165], v[194:209]
	v_mfma_f32_32x32x16_bf16 v[18:33], v[46:49], v[162:165], v[212:227]
	v_mfma_f32_32x32x16_bf16 v[2:17], v[90:93], v[166:169], v[2:17]
	v_mfma_f32_32x32x16_bf16 v[18:33], v[42:45], v[166:169], v[18:33]
	s_nop 7
	v_add_u32_e32 v239, 0x8200, v238
	ds_write_b128 v239, v[130:133] offset:0
	ds_write_b128 v239, v[134:137] offset:16
	ds_write_b128 v239, v[138:141] offset:32
	ds_write_b128 v239, v[142:145] offset:48
	ds_write_b128 v239, v[146:149] offset:128
	ds_write_b128 v239, v[150:153] offset:144
	ds_write_b128 v239, v[154:157] offset:160
	ds_write_b128 v239, v[158:161] offset:176
	v_mfma_f32_32x32x16_bf16 v[2:17], v[86:89], v[170:173], v[2:17]
	ds_read_b128 v[178:181], v236 offset:30208
	v_mfma_f32_32x32x16_bf16 v[18:33], v[38:41], v[170:173], v[18:33]
	ds_read_b128 v[182:185], v236 offset:30240
	v_mfma_f32_32x32x16_bf16 v[2:17], v[82:85], v[174:177], v[2:17]
	ds_read_b128 v[186:189], v236 offset:30272
	v_mfma_f32_32x32x16_bf16 v[18:33], v[34:37], v[174:177], v[18:33]
	ds_read_b128 v[190:193], v236 offset:30304
	s_waitcnt lgkmcnt(0)
	v_mfma_f32_32x32x16_bf16 v[130:145], v[94:97], v[178:181], v[194:209]
	v_mfma_f32_32x32x16_bf16 v[146:161], v[46:49], v[178:181], v[212:227]
	v_mfma_f32_32x32x16_bf16 v[130:145], v[90:93], v[182:185], v[130:145]
	v_mfma_f32_32x32x16_bf16 v[146:161], v[42:45], v[182:185], v[146:161]
	s_nop 7
	v_add_u32_e32 v239, 0x10400, v238
	ds_write_b128 v239, v[2:5] offset:0
	ds_write_b128 v239, v[6:9] offset:16
	ds_write_b128 v239, v[10:13] offset:32
	ds_write_b128 v239, v[14:17] offset:48
	ds_write_b128 v239, v[18:21] offset:128
	ds_write_b128 v239, v[22:25] offset:144
	ds_write_b128 v239, v[26:29] offset:160
	ds_write_b128 v239, v[30:33] offset:176
	v_mfma_f32_32x32x16_bf16 v[130:145], v[86:89], v[186:189], v[130:145]
	v_mfma_f32_32x32x16_bf16 v[146:161], v[38:41], v[186:189], v[146:161]
	v_mfma_f32_32x32x16_bf16 v[130:145], v[82:85], v[190:193], v[130:145]
	v_mfma_f32_32x32x16_bf16 v[146:161], v[34:37], v[190:193], v[146:161]
	s_nop 7
	s_nop 7
	v_cmp_gt_u32_e32 vcc, 16, v228
	s_and_saveexec_b64 s[20:21], vcc
	v_add_u32_e32 v239, 0x18600, v238
	ds_write_b128 v239, v[130:133] offset:0
	ds_write_b128 v239, v[134:137] offset:16
	ds_write_b128 v239, v[138:141] offset:32
	ds_write_b128 v239, v[142:145] offset:48
	ds_write_b128 v239, v[146:149] offset:128
	ds_write_b128 v239, v[150:153] offset:144
	ds_write_b128 v239, v[154:157] offset:160
	ds_write_b128 v239, v[158:161] offset:176
	s_or_b64 exec, exec, s[20:21]
	s_mov_b32 s12, 0xbeb17218
	v_mov_b32_e32 v235, 0xc038aa3b
	v_add_u32_e32 v233, v231, v244
	v_add_u32_e32 v234, v231, v245
	ds_read_b128 v[2:5], v233 offset:0
	ds_read_b128 v[6:9], v233 offset:16
	ds_read_b128 v[10:13], v233 offset:32
	ds_read_b128 v[14:17], v233 offset:48
	ds_read_b128 v[18:21], v233 offset:128
	ds_read_b128 v[22:25], v233 offset:144
	ds_read_b128 v[26:29], v233 offset:160
	ds_read_b128 v[30:33], v233 offset:176
	ds_read_b128 v[34:37], v234 offset:0
	ds_read_b128 v[38:41], v234 offset:16
	ds_read_b128 v[42:45], v234 offset:32
	ds_read_b128 v[46:49], v234 offset:48
	v_mov_b32_e32 v194, 0
	v_mov_b32_e32 v195, 0
	v_mov_b32_e32 v196, 0
	v_mov_b32_e32 v197, 0
	v_mov_b32_e32 v198, 0
	v_mov_b32_e32 v199, 0
	v_mov_b32_e32 v200, 0
	v_mov_b32_e32 v201, 0
	v_mov_b32_e32 v202, 0
	v_mov_b32_e32 v203, 0
	v_mov_b32_e32 v204, 0
	v_mov_b32_e32 v205, 0
	v_mov_b32_e32 v206, 0
	v_mov_b32_e32 v207, 0
	v_mov_b32_e32 v208, 0
	v_mov_b32_e32 v209, 0
	v_add_u32_e32 v232, 0x100, v232
	s_movk_i32 s16, 18
	s_waitcnt vmcnt(0) lgkmcnt(0)
	ds_read_b128 v[82:85], v234 offset:128
	ds_read_b128 v[86:89], v234 offset:144
	ds_read_b128 v[90:93], v234 offset:160
	ds_read_b128 v[94:97], v234 offset:176
	ds_read2_b32 v[244:245], v232 offset1:32
	v_exp_f32_e32 v212, v4
	v_exp_f32_e32 v213, v8
	v_exp_f32_e32 v214, v12
	v_exp_f32_e32 v215, v16
	v_exp_f32_e32 v217, v2
	v_fma_f32 v251, v212, s12, s12
	v_exp_f32_e32 v218, v6
	v_fma_f32 v252, v213, s12, s12
	v_exp_f32_e32 v219, v10
	v_fma_f32 v253, v214, s12, s12
	v_exp_f32_e32 v220, v14
	v_fma_f32 v254, v215, s12, s12
	v_fmac_f32_e32 v251, v217, v251
	v_fmac_f32_e32 v252, v218, v252
	v_fmac_f32_e32 v253, v219, v253
	v_fmac_f32_e32 v254, v220, v254
	v_rcp_f32_e32 v217, v251
	v_rcp_f32_e32 v218, v252
	v_rcp_f32_e32 v219, v253
	v_rcp_f32_e32 v220, v254
	v_exp_f32_e32 v246, v5
	v_fma_f32 v194, -v212, v217, v217
	v_exp_f32_e32 v247, v9
	v_fma_f32 v195, -v213, v218, v218
	v_exp_f32_e32 v248, v13
	v_fma_f32 v196, -v214, v219, v219
	v_exp_f32_e32 v249, v17
	v_fma_f32 v197, -v215, v220, v220
	v_exp_f32_e32 v212, v194
	v_add_f32_e32 v246, 1.0, v246
	v_exp_f32_e32 v213, v195
	v_add_f32_e32 v247, 1.0, v247
	v_exp_f32_e32 v214, v196
	v_add_f32_e32 v248, 1.0, v248
	v_exp_f32_e32 v215, v197
	v_add_f32_e32 v249, 1.0, v249
	v_fmac_f32_e32 v246, v246, v212
	v_fmac_f32_e32 v247, v247, v213
	v_fmac_f32_e32 v248, v248, v214
	v_fmac_f32_e32 v249, v249, v215
	v_rcp_f32_e32 v246, v246
	v_rcp_f32_e32 v247, v247
	v_rcp_f32_e32 v248, v248
	v_rcp_f32_e32 v249, v249
	v_fma_f32 v246, -v212, v246, v246
	v_fma_f32 v247, -v213, v247, v247
	v_fma_f32 v248, -v214, v248, v248
	v_fma_f32 v249, -v215, v249, v249
	v_cvt_pk_bf16_f32 v236, v246, v247
	v_cvt_pk_bf16_f32 v237, v248, v249
	s_waitcnt lgkmcnt(0)
	v_add_u32_e32 v233, v231, v244
	ds_read_b128 v[2:5], v233 offset:0
	ds_read_b128 v[6:9], v233 offset:16
	ds_read_b128 v[10:13], v233 offset:32
	ds_read_b128 v[14:17], v233 offset:48
	v_exp_f32_e32 v212, v20
	v_exp_f32_e32 v213, v24
	v_exp_f32_e32 v214, v28
	v_exp_f32_e32 v215, v32
	v_exp_f32_e32 v217, v18
	v_fma_f32 v251, v212, s12, s12
	v_exp_f32_e32 v218, v22
	v_fma_f32 v252, v213, s12, s12
	v_exp_f32_e32 v219, v26
	v_fma_f32 v253, v214, s12, s12
	v_exp_f32_e32 v220, v30
	v_fma_f32 v254, v215, s12, s12
	v_fmac_f32_e32 v251, v217, v251
	v_fmac_f32_e32 v252, v218, v252
	v_fmac_f32_e32 v253, v219, v253
	v_fmac_f32_e32 v254, v220, v254
	v_rcp_f32_e32 v217, v251
	v_rcp_f32_e32 v218, v252
	v_rcp_f32_e32 v219, v253
	v_rcp_f32_e32 v220, v254
	v_exp_f32_e32 v246, v21
	v_fma_f32 v198, -v212, v217, v217
	v_exp_f32_e32 v247, v25
	v_fma_f32 v199, -v213, v218, v218
	v_exp_f32_e32 v248, v29
	v_fma_f32 v200, -v214, v219, v219
	v_exp_f32_e32 v249, v33
	v_fma_f32 v201, -v215, v220, v220
	v_exp_f32_e32 v212, v198
	v_add_f32_e32 v246, 1.0, v246
	v_exp_f32_e32 v213, v199
	v_add_f32_e32 v247, 1.0, v247
	v_exp_f32_e32 v214, v200
	v_add_f32_e32 v248, 1.0, v248
	v_exp_f32_e32 v215, v201
	v_add_f32_e32 v249, 1.0, v249
	v_fmac_f32_e32 v246, v246, v212
	v_fmac_f32_e32 v247, v247, v213
	v_fmac_f32_e32 v248, v248, v214
	v_fmac_f32_e32 v249, v249, v215
	v_rcp_f32_e32 v246, v246
	v_rcp_f32_e32 v247, v247
	v_rcp_f32_e32 v248, v248
	v_rcp_f32_e32 v249, v249
	v_fma_f32 v246, -v212, v246, v246
	v_fma_f32 v247, -v213, v247, v247
	v_fma_f32 v248, -v214, v248, v248
	v_fma_f32 v249, -v215, v249, v249
	v_cvt_pk_bf16_f32 v238, v246, v247
	v_cvt_pk_bf16_f32 v239, v248, v249
	ds_write_b128 v211, v[236:239] offset:0
	ds_read_b128 v[18:21], v233 offset:128
	ds_read_b128 v[22:25], v233 offset:144
	ds_read_b128 v[26:29], v233 offset:160
	ds_read_b128 v[30:33], v233 offset:176
	v_exp_f32_e32 v212, v36
	v_exp_f32_e32 v213, v40
	v_exp_f32_e32 v214, v44
	v_exp_f32_e32 v215, v48
	s_waitcnt lgkmcnt(4)
	s_barrier
	ds_read_b128 v[130:133], v210 offset:0
	ds_read_b128 v[134:137], v210 offset:1024
	v_exp_f32_e32 v217, v34
	v_fma_f32 v251, v212, s12, s12
	v_exp_f32_e32 v218, v38
	v_fma_f32 v252, v213, s12, s12
	v_exp_f32_e32 v219, v42
	v_fma_f32 v253, v214, s12, s12
	v_exp_f32_e32 v220, v46
	v_fma_f32 v254, v215, s12, s12
	ds_read_b128 v[138:141], v210 offset:2048
	ds_read_b128 v[142:145], v210 offset:3072
	v_fmac_f32_e32 v251, v217, v251
	v_fmac_f32_e32 v252, v218, v252
	v_fmac_f32_e32 v253, v219, v253
	v_fmac_f32_e32 v254, v220, v254
	ds_read_b128 v[146:149], v210 offset:4096
	ds_read_b128 v[150:153], v210 offset:5120
	v_rcp_f32_e32 v217, v251
	v_rcp_f32_e32 v218, v252
	v_rcp_f32_e32 v219, v253
	v_rcp_f32_e32 v220, v254
	ds_read_b128 v[154:157], v210 offset:6144
	ds_read_b128 v[158:161], v210 offset:7168
	v_exp_f32_e32 v246, v37
	v_fma_f32 v202, -v212, v217, v217
	v_exp_f32_e32 v247, v41
	v_fma_f32 v203, -v213, v218, v218
	v_exp_f32_e32 v248, v45
	v_fma_f32 v204, -v214, v219, v219
	v_exp_f32_e32 v249, v49
	v_fma_f32 v205, -v215, v220, v220
	v_exp_f32_e32 v212, v202
	v_add_f32_e32 v246, 1.0, v246
	v_exp_f32_e32 v213, v203
	v_add_f32_e32 v247, 1.0, v247
	v_exp_f32_e32 v214, v204
	v_add_f32_e32 v248, 1.0, v248
	v_exp_f32_e32 v215, v205
	v_add_f32_e32 v249, 1.0, v249
	v_fmac_f32_e32 v246, v246, v212
	v_fmac_f32_e32 v247, v247, v213
	v_fmac_f32_e32 v248, v248, v214
	v_fmac_f32_e32 v249, v249, v215
	v_rcp_f32_e32 v246, v246
	v_rcp_f32_e32 v247, v247
	v_rcp_f32_e32 v248, v248
	v_rcp_f32_e32 v249, v249
	v_fma_f32 v246, -v212, v246, v246
	v_fma_f32 v247, -v213, v247, v247
	v_fma_f32 v248, -v214, v248, v248
	v_fma_f32 v249, -v215, v249, v249
	v_cvt_pk_bf16_f32 v236, v246, v247
	v_cvt_pk_bf16_f32 v237, v248, v249
	s_waitcnt lgkmcnt(0)
	v_mfma_f32_32x32x16_bf16 v[2:17], v[126:129], v[130:133], v[2:17]
	v_add_u32_e32 v234, v231, v245
	ds_read_b128 v[34:37], v234 offset:0
	ds_read_b128 v[38:41], v234 offset:16
	ds_read_b128 v[42:45], v234 offset:32
	ds_read_b128 v[46:49], v234 offset:48
	v_add_u32_e32 v232, 0x100, v232
	v_exp_f32_e32 v212, v84
	v_exp_f32_e32 v213, v88
	v_exp_f32_e32 v214, v92
	v_exp_f32_e32 v215, v96
	v_mfma_f32_32x32x16_bf16 v[2:17], v[122:125], v[134:137], v[2:17]
	v_exp_f32_e32 v217, v82
	v_fma_f32 v251, v212, s12, s12
	v_exp_f32_e32 v218, v86
	v_fma_f32 v252, v213, s12, s12
	v_exp_f32_e32 v219, v90
	v_fma_f32 v253, v214, s12, s12
	v_exp_f32_e32 v220, v94
	v_fma_f32 v254, v215, s12, s12
	v_mfma_f32_32x32x16_bf16 v[2:17], v[118:121], v[138:141], v[2:17]
	v_fmac_f32_e32 v251, v217, v251
	v_fmac_f32_e32 v252, v218, v252
	v_fmac_f32_e32 v253, v219, v253
	v_fmac_f32_e32 v254, v220, v254
	v_mfma_f32_32x32x16_bf16 v[2:17], v[114:117], v[142:145], v[2:17]
	v_rcp_f32_e32 v217, v251
	v_rcp_f32_e32 v218, v252
	v_rcp_f32_e32 v219, v253
	v_rcp_f32_e32 v220, v254
	v_mfma_f32_32x32x16_bf16 v[2:17], v[110:113], v[146:149], v[2:17]
	v_exp_f32_e32 v246, v85
	v_fma_f32 v206, -v212, v217, v217
	v_exp_f32_e32 v247, v89
	v_fma_f32 v207, -v213, v218, v218
	v_exp_f32_e32 v248, v93
	v_fma_f32 v208, -v214, v219, v219
	v_exp_f32_e32 v249, v97
	v_fma_f32 v209, -v215, v220, v220
	v_mfma_f32_32x32x16_bf16 v[2:17], v[106:109], v[150:153], v[2:17]
	v_mfma_f32_32x32x16_bf16 v[2:17], v[102:105], v[154:157], v[2:17]
	v_exp_f32_e32 v212, v206
	v_add_f32_e32 v246, 1.0, v246
	v_exp_f32_e32 v213, v207
	v_add_f32_e32 v247, 1.0, v247
	v_exp_f32_e32 v214, v208
	v_add_f32_e32 v248, 1.0, v248
	v_exp_f32_e32 v215, v209
	v_add_f32_e32 v249, 1.0, v249
	v_fmac_f32_e32 v246, v246, v212
	v_fmac_f32_e32 v247, v247, v213
	v_fmac_f32_e32 v248, v248, v214
	v_fmac_f32_e32 v249, v249, v215
	v_mfma_f32_32x32x16_bf16 v[2:17], v[98:101], v[158:161], v[2:17]
	v_rcp_f32_e32 v246, v246
	v_rcp_f32_e32 v247, v247
	v_rcp_f32_e32 v248, v248
	v_rcp_f32_e32 v249, v249
	v_fma_f32 v246, -v212, v246, v246
	v_fma_f32 v247, -v213, v247, v247
	v_fma_f32 v248, -v214, v248, v248
	v_fma_f32 v249, -v215, v249, v249
	v_cvt_pk_bf16_f32 v238, v246, v247
	v_cvt_pk_bf16_f32 v239, v248, v249
	ds_write_b128 v211, v[236:239] offset:8192
.Llight_loop:
	v_mfma_f32_32x32x16_bf16 v[18:33], v[78:81], v[130:133], v[18:33]
	ds_read_b128 v[82:85], v234 offset:128
	ds_read_b128 v[86:89], v234 offset:144
	ds_read_b128 v[90:93], v234 offset:160
	ds_read_b128 v[94:97], v234 offset:176
	ds_read2_b32 v[244:245], v232 offset1:32
	v_exp_f32_e32 v212, v4
	v_exp_f32_e32 v213, v8
	v_exp_f32_e32 v214, v12
	v_exp_f32_e32 v215, v16
	s_waitcnt lgkmcnt(5)
	s_barrier
	v_mfma_f32_32x32x16_bf16 v[18:33], v[74:77], v[134:137], v[18:33]
	ds_read_b128 v[162:165], v210 offset:8192
	ds_read_b128 v[166:169], v210 offset:9216
	v_exp_f32_e32 v217, v2
	v_fma_f32 v251, v212, s12, s12
	v_exp_f32_e32 v218, v6
	v_fma_f32 v252, v213, s12, s12
	v_exp_f32_e32 v219, v10
	v_fma_f32 v253, v214, s12, s12
	v_exp_f32_e32 v220, v14
	v_fma_f32 v254, v215, s12, s12
	v_mfma_f32_32x32x16_bf16 v[18:33], v[70:73], v[138:141], v[18:33]
	ds_read_b128 v[170:173], v210 offset:10240
	ds_read_b128 v[174:177], v210 offset:11264
	v_exp_f32_e32 v221, v3
	v_fmac_f32_e32 v251, v217, v251
	v_exp_f32_e32 v222, v7
	v_fmac_f32_e32 v252, v218, v252
	v_exp_f32_e32 v223, v11
	v_fmac_f32_e32 v253, v219, v253
	v_exp_f32_e32 v224, v15
	v_fmac_f32_e32 v254, v220, v254
	v_mfma_f32_32x32x16_bf16 v[18:33], v[66:69], v[142:145], v[18:33]
	ds_read_b128 v[178:181], v210 offset:12288
	ds_read_b128 v[182:185], v210 offset:13312
	v_rcp_f32_e32 v217, v251
	v_add_f32_e32 v221, 1.0, v221
	v_rcp_f32_e32 v218, v252
	v_add_f32_e32 v222, 1.0, v222
	v_rcp_f32_e32 v219, v253
	v_add_f32_e32 v223, 1.0, v223
	v_rcp_f32_e32 v220, v254
	v_add_f32_e32 v224, 1.0, v224
	v_mfma_f32_32x32x16_bf16 v[18:33], v[62:65], v[146:149], v[18:33]
	ds_read_b128 v[186:189], v210 offset:14336
	ds_read_b128 v[190:193], v210 offset:15360
	v_rcp_f32_e32 v221, v221
	v_fma_f32 v240, -v212, v217, v217
	v_rcp_f32_e32 v222, v222
	v_fma_f32 v241, -v213, v218, v218
	v_rcp_f32_e32 v223, v223
	v_fma_f32 v242, -v214, v219, v219
	v_rcp_f32_e32 v224, v224
	v_fma_f32 v243, -v215, v220, v220
	v_mfma_f32_32x32x16_bf16 v[18:33], v[58:61], v[150:153], v[18:33]
	v_exp_f32_e32 v246, v5
	v_fma_f32 v194, v221, v194, v240
	v_exp_f32_e32 v247, v9
	v_fma_f32 v195, v222, v195, v241
	v_exp_f32_e32 v248, v13
	v_fma_f32 v196, v223, v196, v242
	v_exp_f32_e32 v249, v17
	v_fma_f32 v197, v224, v197, v243
	v_mfma_f32_32x32x16_bf16 v[18:33], v[54:57], v[154:157], v[18:33]
	v_exp_f32_e32 v212, v194
	v_add_f32_e32 v246, 1.0, v246
	v_exp_f32_e32 v213, v195
	v_add_f32_e32 v247, 1.0, v247
	v_exp_f32_e32 v214, v196
	v_add_f32_e32 v248, 1.0, v248
	v_exp_f32_e32 v215, v197
	v_add_f32_e32 v249, 1.0, v249
	v_fmac_f32_e32 v246, v246, v212
	v_fmac_f32_e32 v247, v247, v213
	v_fmac_f32_e32 v248, v248, v214
	v_fmac_f32_e32 v249, v249, v215
	v_mfma_f32_32x32x16_bf16 v[18:33], v[50:53], v[158:161], v[18:33]
	v_rcp_f32_e32 v246, v246
	v_rcp_f32_e32 v247, v247
	v_rcp_f32_e32 v248, v248
	v_rcp_f32_e32 v249, v249
	v_fma_f32 v246, -v212, v246, v246
	v_fma_f32 v247, -v213, v247, v247
	v_fma_f32 v248, -v214, v248, v248
	v_fma_f32 v249, -v215, v249, v249
	v_cvt_pk_bf16_f32 v236, v246, v247
	v_cvt_pk_bf16_f32 v237, v248, v249
	s_waitcnt lgkmcnt(0)
	v_mfma_f32_32x32x16_bf16 v[34:49], v[126:129], v[162:165], v[34:49]
	v_add_u32_e32 v233, v231, v244
	ds_read_b128 v[2:5], v233 offset:0
	ds_read_b128 v[6:9], v233 offset:16
	ds_read_b128 v[10:13], v233 offset:32
	ds_read_b128 v[14:17], v233 offset:48
	v_exp_f32_e32 v212, v20
	v_exp_f32_e32 v213, v24
	v_exp_f32_e32 v214, v28
	v_exp_f32_e32 v215, v32
	v_mfma_f32_32x32x16_bf16 v[34:49], v[122:125], v[166:169], v[34:49]
	v_exp_f32_e32 v217, v18
	v_fma_f32 v251, v212, s12, s12
	v_exp_f32_e32 v218, v22
	v_fma_f32 v252, v213, s12, s12
	v_exp_f32_e32 v219, v26
	v_fma_f32 v253, v214, s12, s12
	v_exp_f32_e32 v220, v30
	v_fma_f32 v254, v215, s12, s12
	v_mfma_f32_32x32x16_bf16 v[34:49], v[118:121], v[170:173], v[34:49]
	v_exp_f32_e32 v221, v19
	v_fmac_f32_e32 v251, v217, v251
	v_exp_f32_e32 v222, v23
	v_fmac_f32_e32 v252, v218, v252
	v_exp_f32_e32 v223, v27
	v_fmac_f32_e32 v253, v219, v253
	v_exp_f32_e32 v224, v31
	v_fmac_f32_e32 v254, v220, v254
	v_mfma_f32_32x32x16_bf16 v[34:49], v[114:117], v[174:177], v[34:49]
	v_rcp_f32_e32 v217, v251
	v_add_f32_e32 v221, 1.0, v221
	v_rcp_f32_e32 v218, v252
	v_add_f32_e32 v222, 1.0, v222
	v_rcp_f32_e32 v219, v253
	v_add_f32_e32 v223, 1.0, v223
	v_rcp_f32_e32 v220, v254
	v_add_f32_e32 v224, 1.0, v224
	v_mfma_f32_32x32x16_bf16 v[34:49], v[110:113], v[178:181], v[34:49]
	v_rcp_f32_e32 v221, v221
	v_fma_f32 v240, -v212, v217, v217
	v_rcp_f32_e32 v222, v222
	v_fma_f32 v241, -v213, v218, v218
	v_rcp_f32_e32 v223, v223
	v_fma_f32 v242, -v214, v219, v219
	v_rcp_f32_e32 v224, v224
	v_fma_f32 v243, -v215, v220, v220
	v_mfma_f32_32x32x16_bf16 v[34:49], v[106:109], v[182:185], v[34:49]
	v_exp_f32_e32 v246, v21
	v_fma_f32 v198, v221, v198, v240
	v_exp_f32_e32 v247, v25
	v_fma_f32 v199, v222, v199, v241
	v_exp_f32_e32 v248, v29
	v_fma_f32 v200, v223, v200, v242
	v_exp_f32_e32 v249, v33
	v_fma_f32 v201, v224, v201, v243
	v_mfma_f32_32x32x16_bf16 v[34:49], v[102:105], v[186:189], v[34:49]
	v_exp_f32_e32 v212, v198
	v_add_f32_e32 v246, 1.0, v246
	v_exp_f32_e32 v213, v199
	v_add_f32_e32 v247, 1.0, v247
	v_exp_f32_e32 v214, v200
	v_add_f32_e32 v248, 1.0, v248
	v_exp_f32_e32 v215, v201
	v_add_f32_e32 v249, 1.0, v249
	v_fmac_f32_e32 v246, v246, v212
	v_fmac_f32_e32 v247, v247, v213
	v_fmac_f32_e32 v248, v248, v214
	v_fmac_f32_e32 v249, v249, v215
	v_mfma_f32_32x32x16_bf16 v[34:49], v[98:101], v[190:193], v[34:49]
	v_rcp_f32_e32 v246, v246
	v_rcp_f32_e32 v247, v247
	v_rcp_f32_e32 v248, v248
	v_rcp_f32_e32 v249, v249
	v_fma_f32 v246, -v212, v246, v246
	v_fma_f32 v247, -v213, v247, v247
	v_fma_f32 v248, -v214, v248, v248
	v_fma_f32 v249, -v215, v249, v249
	v_cvt_pk_bf16_f32 v238, v246, v247
	v_cvt_pk_bf16_f32 v239, v248, v249
	ds_write_b128 v211, v[236:239] offset:0
	v_mfma_f32_32x32x16_bf16 v[82:97], v[78:81], v[162:165], v[82:97]
	ds_read_b128 v[18:21], v233 offset:128
	ds_read_b128 v[22:25], v233 offset:144
	ds_read_b128 v[26:29], v233 offset:160
	ds_read_b128 v[30:33], v233 offset:176
	v_exp_f32_e32 v212, v36
	v_exp_f32_e32 v213, v40
	v_exp_f32_e32 v214, v44
	v_exp_f32_e32 v215, v48
	s_waitcnt lgkmcnt(4)
	s_barrier
	v_mfma_f32_32x32x16_bf16 v[82:97], v[74:77], v[166:169], v[82:97]
	ds_read_b128 v[130:133], v210 offset:0
	ds_read_b128 v[134:137], v210 offset:1024
	v_exp_f32_e32 v217, v34
	v_fma_f32 v251, v212, s12, s12
	v_exp_f32_e32 v218, v38
	v_fma_f32 v252, v213, s12, s12
	v_exp_f32_e32 v219, v42
	v_fma_f32 v253, v214, s12, s12
	v_exp_f32_e32 v220, v46
	v_fma_f32 v254, v215, s12, s12
	v_mfma_f32_32x32x16_bf16 v[82:97], v[70:73], v[170:173], v[82:97]
	ds_read_b128 v[138:141], v210 offset:2048
	ds_read_b128 v[142:145], v210 offset:3072
	v_exp_f32_e32 v221, v35
	v_fmac_f32_e32 v251, v217, v251
	v_exp_f32_e32 v222, v39
	v_fmac_f32_e32 v252, v218, v252
	v_exp_f32_e32 v223, v43
	v_fmac_f32_e32 v253, v219, v253
	v_exp_f32_e32 v224, v47
	v_fmac_f32_e32 v254, v220, v254
	v_mfma_f32_32x32x16_bf16 v[82:97], v[66:69], v[174:177], v[82:97]
	ds_read_b128 v[146:149], v210 offset:4096
	ds_read_b128 v[150:153], v210 offset:5120
	v_rcp_f32_e32 v217, v251
	v_add_f32_e32 v221, 1.0, v221
	v_rcp_f32_e32 v218, v252
	v_add_f32_e32 v222, 1.0, v222
	v_rcp_f32_e32 v219, v253
	v_add_f32_e32 v223, 1.0, v223
	v_rcp_f32_e32 v220, v254
	v_add_f32_e32 v224, 1.0, v224
	v_mfma_f32_32x32x16_bf16 v[82:97], v[62:65], v[178:181], v[82:97]
	ds_read_b128 v[154:157], v210 offset:6144
	ds_read_b128 v[158:161], v210 offset:7168
	v_rcp_f32_e32 v221, v221
	v_fma_f32 v240, -v212, v217, v217
	v_rcp_f32_e32 v222, v222
	v_fma_f32 v241, -v213, v218, v218
	v_rcp_f32_e32 v223, v223
	v_fma_f32 v242, -v214, v219, v219
	v_rcp_f32_e32 v224, v224
	v_fma_f32 v243, -v215, v220, v220
	v_mfma_f32_32x32x16_bf16 v[82:97], v[58:61], v[182:185], v[82:97]
	v_exp_f32_e32 v246, v37
	v_fma_f32 v202, v221, v202, v240
	v_exp_f32_e32 v247, v41
	v_fma_f32 v203, v222, v203, v241
	v_exp_f32_e32 v248, v45
	v_fma_f32 v204, v223, v204, v242
	v_exp_f32_e32 v249, v49
	v_fma_f32 v205, v224, v205, v243
	v_mfma_f32_32x32x16_bf16 v[82:97], v[54:57], v[186:189], v[82:97]
	v_exp_f32_e32 v212, v202
	v_add_f32_e32 v246, 1.0, v246
	v_exp_f32_e32 v213, v203
	v_add_f32_e32 v247, 1.0, v247
	v_exp_f32_e32 v214, v204
	v_add_f32_e32 v248, 1.0, v248
	v_exp_f32_e32 v215, v205
	v_add_f32_e32 v249, 1.0, v249
	v_fmac_f32_e32 v246, v246, v212
	v_fmac_f32_e32 v247, v247, v213
	v_fmac_f32_e32 v248, v248, v214
	v_fmac_f32_e32 v249, v249, v215
	v_mfma_f32_32x32x16_bf16 v[82:97], v[50:53], v[190:193], v[82:97]
	v_rcp_f32_e32 v246, v246
	v_rcp_f32_e32 v247, v247
	v_rcp_f32_e32 v248, v248
	v_rcp_f32_e32 v249, v249
	v_fma_f32 v246, -v212, v246, v246
	v_fma_f32 v247, -v213, v247, v247
	v_fma_f32 v248, -v214, v248, v248
	v_fma_f32 v249, -v215, v249, v249
	v_cvt_pk_bf16_f32 v236, v246, v247
	v_cvt_pk_bf16_f32 v237, v248, v249
	s_waitcnt lgkmcnt(0)
	v_mfma_f32_32x32x16_bf16 v[2:17], v[126:129], v[130:133], v[2:17]
	v_add_u32_e32 v234, v231, v245
	ds_read_b128 v[34:37], v234 offset:0
	ds_read_b128 v[38:41], v234 offset:16
	ds_read_b128 v[42:45], v234 offset:32
	ds_read_b128 v[46:49], v234 offset:48
	v_add_u32_e32 v232, 0x100, v232
	v_exp_f32_e32 v212, v84
	v_exp_f32_e32 v213, v88
	v_exp_f32_e32 v214, v92
	v_exp_f32_e32 v215, v96
	v_mfma_f32_32x32x16_bf16 v[2:17], v[122:125], v[134:137], v[2:17]
	v_exp_f32_e32 v217, v82
	v_fma_f32 v251, v212, s12, s12
	v_exp_f32_e32 v218, v86
	v_fma_f32 v252, v213, s12, s12
	v_exp_f32_e32 v219, v90
	v_fma_f32 v253, v214, s12, s12
	v_exp_f32_e32 v220, v94
	v_fma_f32 v254, v215, s12, s12
	v_mfma_f32_32x32x16_bf16 v[2:17], v[118:121], v[138:141], v[2:17]
	v_exp_f32_e32 v221, v83
	v_fmac_f32_e32 v251, v217, v251
	v_exp_f32_e32 v222, v87
	v_fmac_f32_e32 v252, v218, v252
	v_exp_f32_e32 v223, v91
	v_fmac_f32_e32 v253, v219, v253
	v_exp_f32_e32 v224, v95
	v_fmac_f32_e32 v254, v220, v254
	v_mfma_f32_32x32x16_bf16 v[2:17], v[114:117], v[142:145], v[2:17]
	v_rcp_f32_e32 v217, v251
	v_add_f32_e32 v221, 1.0, v221
	v_rcp_f32_e32 v218, v252
	v_add_f32_e32 v222, 1.0, v222
	v_rcp_f32_e32 v219, v253
	v_add_f32_e32 v223, 1.0, v223
	v_rcp_f32_e32 v220, v254
	v_add_f32_e32 v224, 1.0, v224
	v_mfma_f32_32x32x16_bf16 v[2:17], v[110:113], v[146:149], v[2:17]
	v_rcp_f32_e32 v221, v221
	v_fma_f32 v240, -v212, v217, v217
	v_rcp_f32_e32 v222, v222
	v_fma_f32 v241, -v213, v218, v218
	v_rcp_f32_e32 v223, v223
	v_fma_f32 v242, -v214, v219, v219
	v_rcp_f32_e32 v224, v224
	v_fma_f32 v243, -v215, v220, v220
	v_mfma_f32_32x32x16_bf16 v[2:17], v[106:109], v[150:153], v[2:17]
	v_exp_f32_e32 v246, v85
	v_fma_f32 v206, v221, v206, v240
	v_exp_f32_e32 v247, v89
	v_fma_f32 v207, v222, v207, v241
	v_exp_f32_e32 v248, v93
	v_fma_f32 v208, v223, v208, v242
	v_exp_f32_e32 v249, v97
	v_fma_f32 v209, v224, v209, v243
	v_mfma_f32_32x32x16_bf16 v[2:17], v[102:105], v[154:157], v[2:17]
	v_exp_f32_e32 v212, v206
	v_add_f32_e32 v246, 1.0, v246
	v_exp_f32_e32 v213, v207
	v_add_f32_e32 v247, 1.0, v247
	v_exp_f32_e32 v214, v208
	v_add_f32_e32 v248, 1.0, v248
	v_exp_f32_e32 v215, v209
	v_add_f32_e32 v249, 1.0, v249
	v_fmac_f32_e32 v246, v246, v212
	v_fmac_f32_e32 v247, v247, v213
	v_fmac_f32_e32 v248, v248, v214
	v_fmac_f32_e32 v249, v249, v215
	v_mfma_f32_32x32x16_bf16 v[2:17], v[98:101], v[158:161], v[2:17]
	v_rcp_f32_e32 v246, v246
	v_rcp_f32_e32 v247, v247
	v_rcp_f32_e32 v248, v248
	v_rcp_f32_e32 v249, v249
	v_fma_f32 v246, -v212, v246, v246
	v_fma_f32 v247, -v213, v247, v247
	v_fma_f32 v248, -v214, v248, v248
	v_fma_f32 v249, -v215, v249, v249
	v_cvt_pk_bf16_f32 v238, v246, v247
	v_cvt_pk_bf16_f32 v239, v248, v249
	ds_write_b128 v211, v[236:239] offset:8192
	s_sub_u32 s16, s16, 1
	s_cmp_lg_u32 s16, 0
	s_cbranch_scc1 .Llight_loop
	v_mfma_f32_32x32x16_bf16 v[18:33], v[78:81], v[130:133], v[18:33]
	ds_read_b128 v[82:85], v234 offset:128
	ds_read_b128 v[86:89], v234 offset:144
	ds_read_b128 v[90:93], v234 offset:160
	ds_read_b128 v[94:97], v234 offset:176
	v_exp_f32_e32 v212, v4
	v_exp_f32_e32 v213, v8
	v_exp_f32_e32 v214, v12
	v_exp_f32_e32 v215, v16
	s_waitcnt lgkmcnt(4)
	s_barrier
	v_mfma_f32_32x32x16_bf16 v[18:33], v[74:77], v[134:137], v[18:33]
	ds_read_b128 v[162:165], v210 offset:8192
	ds_read_b128 v[166:169], v210 offset:9216
	v_exp_f32_e32 v217, v2
	v_fma_f32 v251, v212, s12, s12
	v_exp_f32_e32 v218, v6
	v_fma_f32 v252, v213, s12, s12
	v_exp_f32_e32 v219, v10
	v_fma_f32 v253, v214, s12, s12
	v_exp_f32_e32 v220, v14
	v_fma_f32 v254, v215, s12, s12
	v_mfma_f32_32x32x16_bf16 v[18:33], v[70:73], v[138:141], v[18:33]
	ds_read_b128 v[170:173], v210 offset:10240
	ds_read_b128 v[174:177], v210 offset:11264
	v_exp_f32_e32 v221, v3
	v_fmac_f32_e32 v251, v217, v251
	v_exp_f32_e32 v222, v7
	v_fmac_f32_e32 v252, v218, v252
	v_exp_f32_e32 v223, v11
	v_fmac_f32_e32 v253, v219, v253
	v_exp_f32_e32 v224, v15
	v_fmac_f32_e32 v254, v220, v254
	v_mfma_f32_32x32x16_bf16 v[18:33], v[66:69], v[142:145], v[18:33]
	ds_read_b128 v[178:181], v210 offset:12288
	ds_read_b128 v[182:185], v210 offset:13312
	v_rcp_f32_e32 v217, v251
	v_add_f32_e32 v221, 1.0, v221
	v_rcp_f32_e32 v218, v252
	v_add_f32_e32 v222, 1.0, v222
	v_rcp_f32_e32 v219, v253
	v_add_f32_e32 v223, 1.0, v223
	v_rcp_f32_e32 v220, v254
	v_add_f32_e32 v224, 1.0, v224
	v_mfma_f32_32x32x16_bf16 v[18:33], v[62:65], v[146:149], v[18:33]
	ds_read_b128 v[186:189], v210 offset:14336
	ds_read_b128 v[190:193], v210 offset:15360
	v_rcp_f32_e32 v221, v221
	v_fma_f32 v240, -v212, v217, v217
	v_rcp_f32_e32 v222, v222
	v_fma_f32 v241, -v213, v218, v218
	v_rcp_f32_e32 v223, v223
	v_fma_f32 v242, -v214, v219, v219
	v_rcp_f32_e32 v224, v224
	v_fma_f32 v243, -v215, v220, v220
	v_mfma_f32_32x32x16_bf16 v[18:33], v[58:61], v[150:153], v[18:33]
	v_exp_f32_e32 v246, v5
	v_fma_f32 v194, v221, v194, v240
	v_exp_f32_e32 v247, v9
	v_fma_f32 v195, v222, v195, v241
	v_exp_f32_e32 v248, v13
	v_fma_f32 v196, v223, v196, v242
	v_exp_f32_e32 v249, v17
	v_fma_f32 v197, v224, v197, v243
	v_mfma_f32_32x32x16_bf16 v[18:33], v[54:57], v[154:157], v[18:33]
	v_exp_f32_e32 v212, v194
	v_add_f32_e32 v246, 1.0, v246
	v_exp_f32_e32 v213, v195
	v_add_f32_e32 v247, 1.0, v247
	v_exp_f32_e32 v214, v196
	v_add_f32_e32 v248, 1.0, v248
	v_exp_f32_e32 v215, v197
	v_add_f32_e32 v249, 1.0, v249
	v_fmac_f32_e32 v246, v246, v212
	v_fmac_f32_e32 v247, v247, v213
	v_fmac_f32_e32 v248, v248, v214
	v_fmac_f32_e32 v249, v249, v215
	v_mfma_f32_32x32x16_bf16 v[18:33], v[50:53], v[158:161], v[18:33]
	v_rcp_f32_e32 v246, v246
	v_rcp_f32_e32 v247, v247
	v_rcp_f32_e32 v248, v248
	v_rcp_f32_e32 v249, v249
	v_fma_f32 v246, -v212, v246, v246
	v_fma_f32 v247, -v213, v247, v247
	v_fma_f32 v248, -v214, v248, v248
	v_fma_f32 v249, -v215, v249, v249
	v_cvt_pk_bf16_f32 v236, v246, v247
	v_cvt_pk_bf16_f32 v237, v248, v249
	s_waitcnt lgkmcnt(0)
	v_mfma_f32_32x32x16_bf16 v[34:49], v[126:129], v[162:165], v[34:49]
	v_exp_f32_e32 v212, v20
	v_exp_f32_e32 v213, v24
	v_exp_f32_e32 v214, v28
	v_exp_f32_e32 v215, v32
	v_mfma_f32_32x32x16_bf16 v[34:49], v[122:125], v[166:169], v[34:49]
	v_exp_f32_e32 v217, v18
	v_fma_f32 v251, v212, s12, s12
	v_exp_f32_e32 v218, v22
	v_fma_f32 v252, v213, s12, s12
	v_exp_f32_e32 v219, v26
	v_fma_f32 v253, v214, s12, s12
	v_exp_f32_e32 v220, v30
	v_fma_f32 v254, v215, s12, s12
	v_mfma_f32_32x32x16_bf16 v[34:49], v[118:121], v[170:173], v[34:49]
	v_exp_f32_e32 v221, v19
	v_fmac_f32_e32 v251, v217, v251
	v_exp_f32_e32 v222, v23
	v_fmac_f32_e32 v252, v218, v252
	v_exp_f32_e32 v223, v27
	v_fmac_f32_e32 v253, v219, v253
	v_exp_f32_e32 v224, v31
	v_fmac_f32_e32 v254, v220, v254
	v_mfma_f32_32x32x16_bf16 v[34:49], v[114:117], v[174:177], v[34:49]
	v_rcp_f32_e32 v217, v251
	v_add_f32_e32 v221, 1.0, v221
	v_rcp_f32_e32 v218, v252
	v_add_f32_e32 v222, 1.0, v222
	v_rcp_f32_e32 v219, v253
	v_add_f32_e32 v223, 1.0, v223
	v_rcp_f32_e32 v220, v254
	v_add_f32_e32 v224, 1.0, v224
	v_mfma_f32_32x32x16_bf16 v[34:49], v[110:113], v[178:181], v[34:49]
	v_rcp_f32_e32 v221, v221
	v_fma_f32 v240, -v212, v217, v217
	v_rcp_f32_e32 v222, v222
	v_fma_f32 v241, -v213, v218, v218
	v_rcp_f32_e32 v223, v223
	v_fma_f32 v242, -v214, v219, v219
	v_rcp_f32_e32 v224, v224
	v_fma_f32 v243, -v215, v220, v220
	v_mfma_f32_32x32x16_bf16 v[34:49], v[106:109], v[182:185], v[34:49]
	v_exp_f32_e32 v246, v21
	v_fma_f32 v198, v221, v198, v240
	v_exp_f32_e32 v247, v25
	v_fma_f32 v199, v222, v199, v241
	v_exp_f32_e32 v248, v29
	v_fma_f32 v200, v223, v200, v242
	v_exp_f32_e32 v249, v33
	v_fma_f32 v201, v224, v201, v243
	v_mfma_f32_32x32x16_bf16 v[34:49], v[102:105], v[186:189], v[34:49]
	v_exp_f32_e32 v212, v198
	v_add_f32_e32 v246, 1.0, v246
	v_exp_f32_e32 v213, v199
	v_add_f32_e32 v247, 1.0, v247
	v_exp_f32_e32 v214, v200
	v_add_f32_e32 v248, 1.0, v248
	v_exp_f32_e32 v215, v201
	v_add_f32_e32 v249, 1.0, v249
	v_fmac_f32_e32 v246, v246, v212
	v_fmac_f32_e32 v247, v247, v213
	v_fmac_f32_e32 v248, v248, v214
	v_fmac_f32_e32 v249, v249, v215
	v_mfma_f32_32x32x16_bf16 v[34:49], v[98:101], v[190:193], v[34:49]
	v_rcp_f32_e32 v246, v246
	v_rcp_f32_e32 v247, v247
	v_rcp_f32_e32 v248, v248
	v_rcp_f32_e32 v249, v249
	v_fma_f32 v246, -v212, v246, v246
	v_fma_f32 v247, -v213, v247, v247
	v_fma_f32 v248, -v214, v248, v248
	v_fma_f32 v249, -v215, v249, v249
	v_cvt_pk_bf16_f32 v238, v246, v247
	v_cvt_pk_bf16_f32 v239, v248, v249
	ds_write_b128 v211, v[236:239] offset:0
	s_waitcnt lgkmcnt(0)
	s_barrier
	s_bfe_u32 s20, s19, 0x10006
	s_lshl_b32 s21, s20, 7
	s_lshl_b32 s20, s20, 13
	s_add_u32 s20, s20, 0x30000
	s_add_u32 s22, s14, s20
	s_addc_u32 s23, s15, 0
	s_add_u32 s24, s22, 0x1000
	s_addc_u32 s25, s23, 0
	global_load_dwordx4 v[98:101], v210, s[22:23] offset:0
	global_load_dwordx4 v[102:105], v210, s[22:23] offset:1024
	global_load_dwordx4 v[106:109], v210, s[22:23] offset:2048
	global_load_dwordx4 v[110:113], v210, s[22:23] offset:3072
	global_load_dwordx4 v[114:117], v210, s[24:25] offset:0
	global_load_dwordx4 v[118:121], v210, s[24:25] offset:1024
	global_load_dwordx4 v[122:125], v210, s[24:25] offset:2048
	global_load_dwordx4 v[126:129], v210, s[24:25] offset:3072
	v_or_b32_e32 v250, s21, v230
	global_load_dwordx4 v[130:133], v250, s[4:5] offset:0
	global_load_dwordx4 v[134:137], v250, s[4:5] offset:32
	global_load_dwordx4 v[138:141], v250, s[4:5] offset:64
	global_load_dwordx4 v[142:145], v250, s[4:5] offset:96
	global_load_dwordx4 v[146:149], v250, s[6:7] offset:0
	global_load_dwordx4 v[150:153], v250, s[6:7] offset:32
	global_load_dwordx4 v[154:157], v250, s[6:7] offset:64
	global_load_dwordx4 v[158:161], v250, s[6:7] offset:96
	s_load_dword s26, s[8:9], 0x0
	v_mfma_f32_32x32x16_bf16 v[82:97], v[78:81], v[162:165], v[82:97]
	v_exp_f32_e32 v212, v36
	v_exp_f32_e32 v213, v40
	v_exp_f32_e32 v214, v44
	v_exp_f32_e32 v215, v48
	v_mfma_f32_32x32x16_bf16 v[82:97], v[74:77], v[166:169], v[82:97]
	v_exp_f32_e32 v217, v34
	v_fma_f32 v251, v212, s12, s12
	v_exp_f32_e32 v218, v38
	v_fma_f32 v252, v213, s12, s12
	v_exp_f32_e32 v219, v42
	v_fma_f32 v253, v214, s12, s12
	v_exp_f32_e32 v220, v46
	v_fma_f32 v254, v215, s12, s12
	v_mfma_f32_32x32x16_bf16 v[82:97], v[70:73], v[170:173], v[82:97]
	v_exp_f32_e32 v221, v35
	v_fmac_f32_e32 v251, v217, v251
	v_exp_f32_e32 v222, v39
	v_fmac_f32_e32 v252, v218, v252
	v_exp_f32_e32 v223, v43
	v_fmac_f32_e32 v253, v219, v253
	v_exp_f32_e32 v224, v47
	v_fmac_f32_e32 v254, v220, v254
	v_mfma_f32_32x32x16_bf16 v[82:97], v[66:69], v[174:177], v[82:97]
	v_rcp_f32_e32 v217, v251
	v_add_f32_e32 v221, 1.0, v221
	v_rcp_f32_e32 v218, v252
	v_add_f32_e32 v222, 1.0, v222
	v_rcp_f32_e32 v219, v253
	v_add_f32_e32 v223, 1.0, v223
	v_rcp_f32_e32 v220, v254
	v_add_f32_e32 v224, 1.0, v224
	v_mfma_f32_32x32x16_bf16 v[82:97], v[62:65], v[178:181], v[82:97]
	v_rcp_f32_e32 v221, v221
	v_fma_f32 v240, -v212, v217, v217
	v_rcp_f32_e32 v222, v222
	v_fma_f32 v241, -v213, v218, v218
	v_rcp_f32_e32 v223, v223
	v_fma_f32 v242, -v214, v219, v219
	v_rcp_f32_e32 v224, v224
	v_fma_f32 v243, -v215, v220, v220
	v_mfma_f32_32x32x16_bf16 v[82:97], v[58:61], v[182:185], v[82:97]
	v_exp_f32_e32 v246, v37
	v_fma_f32 v202, v221, v202, v240
	v_exp_f32_e32 v247, v41
	v_fma_f32 v203, v222, v203, v241
	v_exp_f32_e32 v248, v45
	v_fma_f32 v204, v223, v204, v242
	v_exp_f32_e32 v249, v49
	v_fma_f32 v205, v224, v205, v243
	v_mfma_f32_32x32x16_bf16 v[82:97], v[54:57], v[186:189], v[82:97]
	v_exp_f32_e32 v212, v202
	v_add_f32_e32 v246, 1.0, v246
	v_exp_f32_e32 v213, v203
	v_add_f32_e32 v247, 1.0, v247
	v_exp_f32_e32 v214, v204
	v_add_f32_e32 v248, 1.0, v248
	v_exp_f32_e32 v215, v205
	v_add_f32_e32 v249, 1.0, v249
	v_fmac_f32_e32 v246, v246, v212
	v_fmac_f32_e32 v247, v247, v213
	v_fmac_f32_e32 v248, v248, v214
	v_fmac_f32_e32 v249, v249, v215
	v_mfma_f32_32x32x16_bf16 v[82:97], v[50:53], v[190:193], v[82:97]
	v_rcp_f32_e32 v246, v246
	v_rcp_f32_e32 v247, v247
	v_rcp_f32_e32 v248, v248
	v_rcp_f32_e32 v249, v249
	v_fma_f32 v246, -v212, v246, v246
	v_fma_f32 v247, -v213, v247, v247
	v_fma_f32 v248, -v214, v248, v248
	v_fma_f32 v249, -v215, v249, v249
	v_cvt_pk_bf16_f32 v236, v246, v247
	v_cvt_pk_bf16_f32 v237, v248, v249
	s_waitcnt lgkmcnt(0)
	v_exp_f32_e32 v212, v84
	v_exp_f32_e32 v213, v88
	v_exp_f32_e32 v214, v92
	v_exp_f32_e32 v215, v96
	v_exp_f32_e32 v217, v82
	v_fma_f32 v251, v212, s12, s12
	v_exp_f32_e32 v218, v86
	v_fma_f32 v252, v213, s12, s12
	v_exp_f32_e32 v219, v90
	v_fma_f32 v253, v214, s12, s12
	v_exp_f32_e32 v220, v94
	v_fma_f32 v254, v215, s12, s12
	v_exp_f32_e32 v221, v83
	v_fmac_f32_e32 v251, v217, v251
	v_exp_f32_e32 v222, v87
	v_fmac_f32_e32 v252, v218, v252
	v_exp_f32_e32 v223, v91
	v_fmac_f32_e32 v253, v219, v253
	v_exp_f32_e32 v224, v95
	v_fmac_f32_e32 v254, v220, v254
	v_rcp_f32_e32 v217, v251
	v_add_f32_e32 v221, 1.0, v221
	v_rcp_f32_e32 v218, v252
	v_add_f32_e32 v222, 1.0, v222
	v_rcp_f32_e32 v219, v253
	v_add_f32_e32 v223, 1.0, v223
	v_rcp_f32_e32 v220, v254
	v_add_f32_e32 v224, 1.0, v224
	v_rcp_f32_e32 v221, v221
	v_fma_f32 v240, -v212, v217, v217
	v_rcp_f32_e32 v222, v222
	v_fma_f32 v241, -v213, v218, v218
	v_rcp_f32_e32 v223, v223
	v_fma_f32 v242, -v214, v219, v219
	v_rcp_f32_e32 v224, v224
	v_fma_f32 v243, -v215, v220, v220
	v_exp_f32_e32 v246, v85
	v_fma_f32 v206, v221, v206, v240
	v_exp_f32_e32 v247, v89
	v_fma_f32 v207, v222, v207, v241
	v_exp_f32_e32 v248, v93
	v_fma_f32 v208, v223, v208, v242
	v_exp_f32_e32 v249, v97
	v_fma_f32 v209, v224, v209, v243
	v_exp_f32_e32 v212, v206
	v_add_f32_e32 v246, 1.0, v246
	v_exp_f32_e32 v213, v207
	v_add_f32_e32 v247, 1.0, v247
	v_exp_f32_e32 v214, v208
	v_add_f32_e32 v248, 1.0, v248
	v_exp_f32_e32 v215, v209
	v_add_f32_e32 v249, 1.0, v249
	v_fmac_f32_e32 v246, v246, v212
	v_fmac_f32_e32 v247, v247, v213
	v_fmac_f32_e32 v248, v248, v214
	v_fmac_f32_e32 v249, v249, v215
	v_rcp_f32_e32 v246, v246
	v_rcp_f32_e32 v247, v247
	v_rcp_f32_e32 v248, v248
	v_rcp_f32_e32 v249, v249
	v_fma_f32 v246, -v212, v246, v246
	v_fma_f32 v247, -v213, v247, v247
	v_fma_f32 v248, -v214, v248, v248
	v_fma_f32 v249, -v215, v249, v249
	v_cvt_pk_bf16_f32 v238, v246, v247
	v_cvt_pk_bf16_f32 v239, v248, v249
	ds_write_b128 v211, v[236:239] offset:8192
	s_waitcnt lgkmcnt(0)
	s_barrier
	s_lshl_b32 s20, s19, 6
	s_and_b32 s20, s20, 0x2000
	v_or_b32_e32 v20, s20, v210
	ds_read_b128 v[162:165], v20 offset:0
	ds_read_b128 v[166:169], v20 offset:1024
	ds_read_b128 v[170:173], v20 offset:2048
	ds_read_b128 v[174:177], v20 offset:3072
	ds_read_b128 v[178:181], v20 offset:4096
	ds_read_b128 v[182:185], v20 offset:5120
	ds_read_b128 v[186:189], v20 offset:6144
	ds_read_b128 v[190:193], v20 offset:7168
	s_bfe_u32 s20, s19, 0x10006
	s_lshl_b32 s20, s20, 9
	s_and_b32 s21, s19, 0x80
	s_or_b32 s20, s20, s21
	v_lshlrev_b32_e32 v19, 2, v229
	v_add3_u32 v19, s20, v19, v228
	s_waitcnt vmcnt(0)
	s_waitcnt lgkmcnt(7)
	v_mfma_f32_32x32x16_bf16 v[2:17], v[98:101], v[162:165], 0
	s_waitcnt lgkmcnt(6)
	v_mfma_f32_32x32x16_bf16 v[2:17], v[102:105], v[166:169], v[2:17]
	s_waitcnt lgkmcnt(5)
	v_mfma_f32_32x32x16_bf16 v[2:17], v[106:109], v[170:173], v[2:17]
	s_waitcnt lgkmcnt(4)
	v_mfma_f32_32x32x16_bf16 v[2:17], v[110:113], v[174:177], v[2:17]
	s_waitcnt lgkmcnt(3)
	v_mfma_f32_32x32x16_bf16 v[2:17], v[114:117], v[178:181], v[2:17]
	s_waitcnt lgkmcnt(2)
	v_mfma_f32_32x32x16_bf16 v[2:17], v[118:121], v[182:185], v[2:17]
	s_waitcnt lgkmcnt(1)
	v_mfma_f32_32x32x16_bf16 v[2:17], v[122:125], v[186:189], v[2:17]
	s_waitcnt lgkmcnt(0)
	v_mfma_f32_32x32x16_bf16 v[2:17], v[126:129], v[190:193], v[2:17]
	s_nop 15
	s_nop 3
	v_add_f32_e32 v2, v2, v130
	v_add_f32_e32 v3, v3, v131
	v_add_f32_e32 v4, v4, v132
	v_add_f32_e32 v5, v5, v133
	v_add_f32_e32 v6, v6, v134
	v_add_f32_e32 v7, v7, v135
	v_add_f32_e32 v8, v8, v136
	v_add_f32_e32 v9, v9, v137
	v_add_f32_e32 v10, v10, v138
	v_add_f32_e32 v11, v11, v139
	v_add_f32_e32 v12, v12, v140
	v_add_f32_e32 v13, v13, v141
	v_add_f32_e32 v14, v14, v142
	v_add_f32_e32 v15, v15, v143
	v_add_f32_e32 v16, v16, v144
	v_add_f32_e32 v17, v17, v145
	v_max_f32_e32 v2, 0, v2
	v_max_f32_e32 v3, 0, v3
	v_max_f32_e32 v4, 0, v4
	v_max_f32_e32 v5, 0, v5
	v_max_f32_e32 v6, 0, v6
	v_max_f32_e32 v7, 0, v7
	v_max_f32_e32 v8, 0, v8
	v_max_f32_e32 v9, 0, v9
	v_max_f32_e32 v10, 0, v10
	v_max_f32_e32 v11, 0, v11
	v_max_f32_e32 v12, 0, v12
	v_max_f32_e32 v13, 0, v13
	v_max_f32_e32 v14, 0, v14
	v_max_f32_e32 v15, 0, v15
	v_max_f32_e32 v16, 0, v16
	v_max_f32_e32 v17, 0, v17
	v_fma_f32 v18, v2, v146, 0
	v_fmac_f32_e32 v18, v3, v147
	v_fmac_f32_e32 v18, v4, v148
	v_fmac_f32_e32 v18, v5, v149
	v_fmac_f32_e32 v18, v6, v150
	v_fmac_f32_e32 v18, v7, v151
	v_fmac_f32_e32 v18, v8, v152
	v_fmac_f32_e32 v18, v9, v153
	v_fmac_f32_e32 v18, v10, v154
	v_fmac_f32_e32 v18, v11, v155
	v_fmac_f32_e32 v18, v12, v156
	v_fmac_f32_e32 v18, v13, v157
	v_fmac_f32_e32 v18, v14, v158
	v_fmac_f32_e32 v18, v15, v159
	v_fmac_f32_e32 v18, v16, v160
	v_fmac_f32_e32 v18, v17, v161
	ds_write_b32 v19, v18 offset:35904
	s_branch .LBB1_40
